# gemm2: epilogue gate loads issued before the K-loop's final barrier (exit path), latency overlaps the rendezvous
# baseline (speedup 1.0000x reference)
; #define PG8_STAGE(bufoff, gbase, voff) do { _Pragma("unroll") for (int _i = 0; _i < 2; ++_i) \
;         __builtin_amdgcn_global_load_lds((const unsigned*)((const char*)(gbase) + (voff)[_i]), (LAS unsigned*)(lds + (bufoff) + ldsw + _i * 8192), 16, 0, 0); } while (0)
; #define PG8_LDA(dst, b, h) do { _Pragma("unroll") for (int m = 0; m < 4; ++m) _Pragma("unroll") for (int k = 0; k < 2; ++k) dst[m][k] = *(const LAS bf16x8*)(lds + PG8_SA(b, h) + aoff + m * 2048 + k * 1024); } while (0)
; #define PG8_LDB(dst, b, h) do { _Pragma("unroll") for (int n = 0; n < 2; ++n) _Pragma("unroll") for (int k = 0; k < 2; ++k) dst[n][k] = *(const LAS bf16x8*)(lds + PG8_SB(b, h) + boff + n * 2048 + k * 1024); } while (0)
; #define PG8_MMA(ai, bj, At, Bt) do { __builtin_amdgcn_s_setprio(1); _Pragma("unroll") for (int m = 0; m < 4; ++m) _Pragma("unroll") for (int n = 0; n < 2; ++n) _Pragma("unroll") for (int k = 0; k < 2; ++k) \
;         acc[ai][bj][m][n] = __builtin_amdgcn_mfma_f32_16x16x32_bf16(Bt[n][k], At[m][k], acc[ai][bj][m][n], 0, 0, 0); __builtin_amdgcn_s_setprio(0); } while (0)
; #define PG8_WAIT_V(n) asm volatile("s_waitcnt vmcnt(" #n ")" ::: "memory")
; #define PG8_WAIT_L(n) asm volatile("s_waitcnt lgkmcnt(" #n ")" ::: "memory")
; #define PG8_BAR __builtin_amdgcn_s_barrier()
; #define PG8_SCHED __builtin_amdgcn_sched_barrier(0)
; template <class Epi, class Sched>
; __device__ __forceinline__ void gemm_phase(LAS unsigned char* lds, const bf16_t* Abase, const int K, const Sched& S, const Epi& E, const int wvid) {
;     ...
;             PG8_LDB(B0, 0, 0); PG8_SCHED; PG8_LDA(At, 0, 0); PG8_STAGE(PG8_SA(1, 1), a1, voffA[1]);
;             PG8_WAIT_L(8); PG8_BAR; PG8_WAIT_L(0); PG8_MMA(0, 0, At, B0); PG8_BAR; PG8_SCHED;
;             if (last && has_next) PG8_AOFF(nxt);
;             const char* a2 = last ? Ab : Ab + (size_t)(t + 2) * kstep; const char* b2 = last ? nB : cB + (size_t)(t + 2) * kstep;
;             const char* a3 = a2 + kstep; const char* b3 = b2 + kstep;
;             PG8_LDB(B1, 0, 1); PG8_STAGE(PG8_SB(0, 0), b2, voffB);
;             PG8_BAR; PG8_WAIT_L(0); PG8_MMA(0, 1, At, B1); PG8_BAR;
;             PG8_LDA(At, 0, 1); PG8_STAGE(PG8_SA(0, 0), a2, voffA[0]);
;             PG8_BAR; PG8_WAIT_L(0); PG8_MMA(1, 0, At, B0); PG8_BAR; PG8_SCHED;
;             PG8_STAGE(PG8_SB(0, 1), b2 + hstep, voffB);
;             PG8_WAIT_V(6); PG8_BAR; PG8_MMA(1, 1, At, B1); PG8_BAR;
.LBB0_1479:
	s_add_u32 s28, s26, 0x100
	s_addc_u32 s29, s27, 0
	s_and_b64 s[30:31], s[4:5], exec
	s_cselect_b32 s30, 0, s28
	s_cselect_b32 s31, 0, s29
	s_add_u32 s30, s10, s30
	v_lshl_add_u64 v[236:237], v[196:197], 0, s[26:27]
	s_addc_u32 s31, s11, s31
	s_add_i32 s26, 0, 0x14000
	v_cndmask_b32_e64 v237, v237, v191, s[4:5]
	v_cndmask_b32_e64 v236, v236, v229, s[4:5]
	s_mov_b32 m0, s39
	v_add_u32_e32 v185, s26, v223
	v_lshl_add_u64 v[238:239], v[236:237], 0, v[180:181]
	ds_read_b128 v[200:203], v185
	ds_read_b128 v[206:209], v185 offset:1024
	ds_read_b128 v[210:213], v185 offset:2048
	ds_read_b128 v[232:235], v185 offset:3072
	global_load_lds_dwordx4 v[238:239], off
	v_lshl_add_u64 v[240:241], v[236:237], 0, v[182:183]
	s_mov_b32 m0, s42
	s_nop 0
	global_load_lds_dwordx4 v[240:241], off
	s_barrier
	s_waitcnt lgkmcnt(0)
	s_waitcnt lgkmcnt(0)
	v_mfma_f32_16x16x32_bf16 v[94:97], v[200:203], v[170:173], v[94:97]
	v_mfma_f32_16x16x32_bf16 v[90:93], v[210:213], v[170:173], v[90:93]
	v_mfma_f32_16x16x32_bf16 v[86:89], v[200:203], v[162:165], v[86:89]
	v_mfma_f32_16x16x32_bf16 v[82:85], v[210:213], v[162:165], v[82:85]
	v_mfma_f32_16x16x32_bf16 v[78:81], v[200:203], v[154:157], v[78:81]
	v_mfma_f32_16x16x32_bf16 v[74:77], v[210:213], v[154:157], v[74:77]
	v_mfma_f32_16x16x32_bf16 v[70:73], v[200:203], v[146:149], v[70:73]
	v_mfma_f32_16x16x32_bf16 v[66:69], v[210:213], v[146:149], v[66:69]
	v_mfma_f32_16x16x32_bf16 v[94:97], v[206:209], v[174:177], v[94:97]
	v_mfma_f32_16x16x32_bf16 v[90:93], v[232:235], v[174:177], v[90:93]
	v_mfma_f32_16x16x32_bf16 v[86:89], v[206:209], v[166:169], v[86:89]
	v_mfma_f32_16x16x32_bf16 v[82:85], v[232:235], v[166:169], v[82:85]
	v_mfma_f32_16x16x32_bf16 v[78:81], v[206:209], v[158:161], v[78:81]
	v_mfma_f32_16x16x32_bf16 v[74:77], v[232:235], v[158:161], v[74:77]
	v_mfma_f32_16x16x32_bf16 v[70:73], v[206:209], v[150:153], v[70:73]
	v_mfma_f32_16x16x32_bf16 v[66:69], v[232:235], v[150:153], v[66:69]
	s_mov_b32 m0, s17
	s_barrier
	ds_read_b128 v[146:149], v225 offset:16384
	ds_read_b128 v[150:153], v225 offset:17408
	ds_read_b128 v[154:157], v225 offset:18432
	ds_read_b128 v[158:161], v225 offset:19456
	ds_read_b128 v[162:165], v225 offset:20480
	ds_read_b128 v[166:169], v225 offset:21504
	ds_read_b128 v[170:173], v225 offset:22528
	ds_read_b128 v[174:177], v225 offset:23552
	global_load_lds_dwordx4 v0, s[30:31]
	s_mov_b32 m0, s43
	v_mov_b32_e32 v187, v1
	global_load_lds_dwordx4 v186, s[30:31]
	s_barrier
	s_waitcnt lgkmcnt(0)
	v_lshl_add_u64 v[242:243], s[30:31], 0, v[0:1]
	v_lshl_add_u64 v[244:245], s[30:31], 0, v[186:187]
	s_waitcnt lgkmcnt(0)
	v_mfma_f32_16x16x32_bf16 v[62:65], v[130:133], v[146:149], v[62:65]
	v_mfma_f32_16x16x32_bf16 v[58:61], v[138:141], v[146:149], v[58:61]
	v_mfma_f32_16x16x32_bf16 v[46:49], v[130:133], v[154:157], v[46:49]
	v_mfma_f32_16x16x32_bf16 v[42:45], v[138:141], v[154:157], v[42:45]
	v_mfma_f32_16x16x32_bf16 v[30:33], v[130:133], v[162:165], v[30:33]
	v_mfma_f32_16x16x32_bf16 v[26:29], v[138:141], v[162:165], v[26:29]
	v_mfma_f32_16x16x32_bf16 v[14:17], v[130:133], v[170:173], v[14:17]
	v_mfma_f32_16x16x32_bf16 v[10:13], v[138:141], v[170:173], v[10:13]
	v_mfma_f32_16x16x32_bf16 v[62:65], v[134:137], v[150:153], v[62:65]
	v_mfma_f32_16x16x32_bf16 v[58:61], v[142:145], v[150:153], v[58:61]
	v_mfma_f32_16x16x32_bf16 v[46:49], v[134:137], v[158:161], v[46:49]
	v_mfma_f32_16x16x32_bf16 v[42:45], v[142:145], v[158:161], v[42:45]
	v_mfma_f32_16x16x32_bf16 v[30:33], v[134:137], v[166:169], v[30:33]
	v_mfma_f32_16x16x32_bf16 v[26:29], v[142:145], v[166:169], v[26:29]
	v_mfma_f32_16x16x32_bf16 v[14:17], v[134:137], v[174:177], v[14:17]
	v_mfma_f32_16x16x32_bf16 v[10:13], v[142:145], v[174:177], v[10:13]
	s_barrier
	v_lshl_add_u64 v[130:131], v[236:237], 0, s[68:69]
	s_add_i32 s4, s26, s38
	v_lshl_add_u64 v[132:133], v[130:131], 0, v[180:181]
	s_mov_b32 m0, s4
	v_lshl_add_u64 v[130:131], v[130:131], 0, v[182:183]
	global_load_lds_dwordx4 v[132:133], off
	s_add_i32 m0, s4, 0x2000
	s_nop 0
	global_load_lds_dwordx4 v[130:131], off
	s_waitcnt vmcnt(6)
	s_barrier
	v_mfma_f32_16x16x32_bf16 v[54:57], v[200:203], v[146:149], v[54:57]
	v_mfma_f32_16x16x32_bf16 v[50:53], v[210:213], v[146:149], v[50:53]
	v_mfma_f32_16x16x32_bf16 v[38:41], v[200:203], v[154:157], v[38:41]
	v_mfma_f32_16x16x32_bf16 v[34:37], v[210:213], v[154:157], v[34:37]
	v_mfma_f32_16x16x32_bf16 v[22:25], v[200:203], v[162:165], v[22:25]
	v_mfma_f32_16x16x32_bf16 v[18:21], v[210:213], v[162:165], v[18:21]
	v_mfma_f32_16x16x32_bf16 v[6:9], v[200:203], v[170:173], v[6:9]
	v_mfma_f32_16x16x32_bf16 v[2:5], v[210:213], v[170:173], v[2:5]
	v_mfma_f32_16x16x32_bf16 v[54:57], v[206:209], v[150:153], v[54:57]
	v_mfma_f32_16x16x32_bf16 v[50:53], v[232:235], v[150:153], v[50:53]
	v_mfma_f32_16x16x32_bf16 v[38:41], v[206:209], v[158:161], v[38:41]
	v_mfma_f32_16x16x32_bf16 v[34:37], v[232:235], v[158:161], v[34:37]
	v_mfma_f32_16x16x32_bf16 v[22:25], v[206:209], v[166:169], v[22:25]
	v_mfma_f32_16x16x32_bf16 v[18:21], v[232:235], v[166:169], v[18:21]
	v_mfma_f32_16x16x32_bf16 v[6:9], v[206:209], v[174:177], v[6:9]
	v_mfma_f32_16x16x32_bf16 v[2:5], v[232:235], v[174:177], v[2:5]
	s_add_i32 s4, 0, 0x18000
	v_add_u32_e32 v142, s4, v223
	s_barrier
	ds_read_b128 v[130:133], v142
	ds_read_b128 v[134:137], v142 offset:1024
	ds_read_b128 v[138:141], v142 offset:2048
	ds_read_b128 v[142:145], v142 offset:3072
	s_mov_b32 m0, s46
	v_lshl_add_u64 v[198:199], s[30:31], 0, v[198:199]
	ds_read_b128 v[146:149], v225 offset:32768
	ds_read_b128 v[150:153], v225 offset:33792
	ds_read_b128 v[154:157], v225 offset:34816
	ds_read_b128 v[158:161], v225 offset:35840
	ds_read_b128 v[162:165], v225 offset:36864
	ds_read_b128 v[166:169], v225 offset:37888
	ds_read_b128 v[170:173], v225 offset:38912
	ds_read_b128 v[174:177], v225 offset:39936
	global_load_lds_dwordx4 v[198:199], off
	v_lshl_add_u64 v[198:199], s[30:31], 0, v[188:189]
	s_mov_b32 m0, s47
	s_nop 0
	global_load_lds_dwordx4 v[198:199], off
	s_waitcnt lgkmcnt(8)
	s_barrier
; #define PG8_STAGE(bufoff, gbase, voff) do { _Pragma("unroll") for (int _i = 0; _i < 2; ++_i) \
;         __builtin_amdgcn_global_load_lds((const unsigned*)((const char*)(gbase) + (voff)[_i]), (LAS unsigned*)(lds + (bufoff) + ldsw + _i * 8192), 16, 0, 0); } while (0)
; #define PG8_LDA(dst, b, h) do { _Pragma("unroll") for (int m = 0; m < 4; ++m) _Pragma("unroll") for (int k = 0; k < 2; ++k) dst[m][k] = *(const LAS bf16x8*)(lds + PG8_SA(b, h) + aoff + m * 2048 + k * 1024); } while (0)
; #define PG8_LDB(dst, b, h) do { _Pragma("unroll") for (int n = 0; n < 2; ++n) _Pragma("unroll") for (int k = 0; k < 2; ++k) dst[n][k] = *(const LAS bf16x8*)(lds + PG8_SB(b, h) + boff + n * 2048 + k * 1024); } while (0)
; #define PG8_MMA(ai, bj, At, Bt) do { __builtin_amdgcn_s_setprio(1); _Pragma("unroll") for (int m = 0; m < 4; ++m) _Pragma("unroll") for (int n = 0; n < 2; ++n) _Pragma("unroll") for (int k = 0; k < 2; ++k) \
;         acc[ai][bj][m][n] = __builtin_amdgcn_mfma_f32_16x16x32_bf16(Bt[n][k], At[m][k], acc[ai][bj][m][n], 0, 0, 0); __builtin_amdgcn_s_setprio(0); } while (0)
; #define PG8_WAIT_V(n) asm volatile("s_waitcnt vmcnt(" #n ")" ::: "memory")
; #define PG8_WAIT_L(n) asm volatile("s_waitcnt lgkmcnt(" #n ")" ::: "memory")
; #define PG8_BAR __builtin_amdgcn_s_barrier()
; #define PG8_SCHED __builtin_amdgcn_sched_barrier(0)
; template <class Epi, class Sched>
; __device__ __forceinline__ void gemm_phase(LAS unsigned char* lds, const bf16_t* Abase, const int K, const Sched& S, const Epi& E, const int wvid) {
;     ...
;             PG8_LDB(B0, 1, 0); PG8_SCHED; PG8_LDA(At, 1, 0); PG8_STAGE(PG8_SA(0, 1), a2, voffA[1]);
;             PG8_WAIT_L(8); PG8_BAR; PG8_WAIT_L(0); PG8_MMA(0, 0, At, B0); PG8_BAR; PG8_SCHED;
;             PG8_LDB(B1, 1, 1); PG8_STAGE(PG8_SB(1, 0), b3, voffB);
;             PG8_BAR; PG8_WAIT_L(0); PG8_MMA(0, 1, At, B1); PG8_BAR;
;             PG8_LDA(At, 1, 1); PG8_STAGE(PG8_SA(1, 0), a3, voffA[0]);
;             PG8_BAR; PG8_WAIT_L(0); PG8_MMA(1, 0, At, B0); PG8_BAR; PG8_SCHED;
;             PG8_STAGE(PG8_SB(1, 1), b3 + hstep, voffB);
;             PG8_WAIT_V(6); PG8_BAR; PG8_MMA(1, 1, At, B1); PG8_BAR;
;         }
	s_waitcnt lgkmcnt(0)
	s_waitcnt lgkmcnt(0)
	v_mfma_f32_16x16x32_bf16 v[126:129], v[130:133], v[146:149], v[126:129]
	v_mfma_f32_16x16x32_bf16 v[122:125], v[138:141], v[146:149], v[122:125]
	v_mfma_f32_16x16x32_bf16 v[118:121], v[130:133], v[154:157], v[118:121]
	v_mfma_f32_16x16x32_bf16 v[114:117], v[138:141], v[154:157], v[114:117]
	v_mfma_f32_16x16x32_bf16 v[110:113], v[130:133], v[162:165], v[110:113]
	v_mfma_f32_16x16x32_bf16 v[106:109], v[138:141], v[162:165], v[106:109]
	v_mfma_f32_16x16x32_bf16 v[102:105], v[130:133], v[170:173], v[102:105]
	v_mfma_f32_16x16x32_bf16 v[98:101], v[138:141], v[170:173], v[98:101]
	v_mfma_f32_16x16x32_bf16 v[126:129], v[134:137], v[150:153], v[126:129]
	v_mfma_f32_16x16x32_bf16 v[122:125], v[142:145], v[150:153], v[122:125]
	v_mfma_f32_16x16x32_bf16 v[118:121], v[134:137], v[158:161], v[118:121]
	v_mfma_f32_16x16x32_bf16 v[114:117], v[142:145], v[158:161], v[114:117]
	v_mfma_f32_16x16x32_bf16 v[110:113], v[134:137], v[166:169], v[110:113]
	v_mfma_f32_16x16x32_bf16 v[106:109], v[142:145], v[166:169], v[106:109]
	v_mfma_f32_16x16x32_bf16 v[102:105], v[134:137], v[174:177], v[102:105]
	v_mfma_f32_16x16x32_bf16 v[98:101], v[142:145], v[174:177], v[98:101]
	s_barrier
	s_add_i32 s5, 0, 0x1c000
	s_add_i32 s4, s4, s38
	v_add_u32_e32 v185, s5, v223
	v_lshl_add_u64 v[202:203], v[238:239], 0, s[12:13]
	s_mov_b32 m0, s4
	ds_read_b128 v[198:201], v185
	ds_read_b128 v[206:209], v185 offset:1024
	ds_read_b128 v[210:213], v185 offset:2048
	ds_read_b128 v[232:235], v185 offset:3072
	global_load_lds_dwordx4 v[202:203], off
	v_lshl_add_u64 v[202:203], v[240:241], 0, s[12:13]
	s_add_i32 m0, s4, 0x2000
	s_nop 0
	global_load_lds_dwordx4 v[202:203], off
	s_barrier
	s_waitcnt lgkmcnt(0)
	s_waitcnt lgkmcnt(0)
	v_mfma_f32_16x16x32_bf16 v[94:97], v[198:201], v[146:149], v[94:97]
	v_mfma_f32_16x16x32_bf16 v[90:93], v[210:213], v[146:149], v[90:93]
	v_mfma_f32_16x16x32_bf16 v[86:89], v[198:201], v[154:157], v[86:89]
	v_mfma_f32_16x16x32_bf16 v[82:85], v[210:213], v[154:157], v[82:85]
	v_mfma_f32_16x16x32_bf16 v[78:81], v[198:201], v[162:165], v[78:81]
	v_mfma_f32_16x16x32_bf16 v[74:77], v[210:213], v[162:165], v[74:77]
	v_mfma_f32_16x16x32_bf16 v[70:73], v[198:201], v[170:173], v[70:73]
	v_mfma_f32_16x16x32_bf16 v[66:69], v[210:213], v[170:173], v[66:69]
	v_mfma_f32_16x16x32_bf16 v[94:97], v[206:209], v[150:153], v[94:97]
	v_mfma_f32_16x16x32_bf16 v[90:93], v[232:235], v[150:153], v[90:93]
	v_mfma_f32_16x16x32_bf16 v[86:89], v[206:209], v[158:161], v[86:89]
	v_mfma_f32_16x16x32_bf16 v[82:85], v[232:235], v[158:161], v[82:85]
	v_mfma_f32_16x16x32_bf16 v[78:81], v[206:209], v[166:169], v[78:81]
	v_mfma_f32_16x16x32_bf16 v[74:77], v[232:235], v[166:169], v[74:77]
	v_mfma_f32_16x16x32_bf16 v[70:73], v[206:209], v[174:177], v[70:73]
	v_mfma_f32_16x16x32_bf16 v[66:69], v[232:235], v[174:177], v[66:69]
	s_mov_b32 m0, s48
	v_lshl_add_u64 v[202:203], v[242:243], 0, s[12:13]
	s_barrier
	ds_read_b128 v[146:149], v225 offset:49152
	ds_read_b128 v[150:153], v225 offset:50176
	ds_read_b128 v[154:157], v225 offset:51200
	ds_read_b128 v[158:161], v225 offset:52224
	ds_read_b128 v[162:165], v225 offset:53248
	ds_read_b128 v[166:169], v225 offset:54272
	ds_read_b128 v[170:173], v225 offset:55296
	ds_read_b128 v[174:177], v225 offset:56320
	global_load_lds_dwordx4 v[202:203], off
	v_lshl_add_u64 v[202:203], v[244:245], 0, s[12:13]
	s_mov_b32 m0, s49
	s_nop 0
	global_load_lds_dwordx4 v[202:203], off
	s_barrier
	s_waitcnt lgkmcnt(0)
	s_waitcnt lgkmcnt(0)
	v_mfma_f32_16x16x32_bf16 v[62:65], v[130:133], v[146:149], v[62:65]
	v_mfma_f32_16x16x32_bf16 v[58:61], v[138:141], v[146:149], v[58:61]
	v_mfma_f32_16x16x32_bf16 v[46:49], v[130:133], v[154:157], v[46:49]
	v_mfma_f32_16x16x32_bf16 v[42:45], v[138:141], v[154:157], v[42:45]
	v_mfma_f32_16x16x32_bf16 v[30:33], v[130:133], v[162:165], v[30:33]
	v_mfma_f32_16x16x32_bf16 v[26:29], v[138:141], v[162:165], v[26:29]
	v_mfma_f32_16x16x32_bf16 v[14:17], v[130:133], v[170:173], v[14:17]
	v_mfma_f32_16x16x32_bf16 v[10:13], v[138:141], v[170:173], v[10:13]
	v_mfma_f32_16x16x32_bf16 v[62:65], v[134:137], v[150:153], v[62:65]
	v_mfma_f32_16x16x32_bf16 v[58:61], v[142:145], v[150:153], v[58:61]
	v_mfma_f32_16x16x32_bf16 v[46:49], v[134:137], v[158:161], v[46:49]
	v_mfma_f32_16x16x32_bf16 v[42:45], v[142:145], v[158:161], v[42:45]
	v_mfma_f32_16x16x32_bf16 v[30:33], v[134:137], v[166:169], v[30:33]
	v_mfma_f32_16x16x32_bf16 v[26:29], v[142:145], v[166:169], v[26:29]
	v_mfma_f32_16x16x32_bf16 v[14:17], v[134:137], v[174:177], v[14:17]
	v_mfma_f32_16x16x32_bf16 v[10:13], v[142:145], v[174:177], v[10:13]
	s_barrier
	v_lshl_add_u64 v[130:131], v[236:237], 0, s[84:85]
	s_add_i32 s4, s5, s38
	v_lshl_add_u64 v[132:133], v[130:131], 0, v[180:181]
	s_mov_b32 m0, s4
	v_lshl_add_u64 v[130:131], v[130:131], 0, v[182:183]
	global_load_lds_dwordx4 v[132:133], off
	s_add_i32 m0, s4, 0x2000
	s_nop 0
	global_load_lds_dwordx4 v[130:131], off
	s_waitcnt vmcnt(6)
	s_barrier
	v_mfma_f32_16x16x32_bf16 v[54:57], v[198:201], v[146:149], v[54:57]
	v_mfma_f32_16x16x32_bf16 v[50:53], v[210:213], v[146:149], v[50:53]
	v_mfma_f32_16x16x32_bf16 v[38:41], v[198:201], v[154:157], v[38:41]
	v_mfma_f32_16x16x32_bf16 v[34:37], v[210:213], v[154:157], v[34:37]
	v_mfma_f32_16x16x32_bf16 v[22:25], v[198:201], v[162:165], v[22:25]
	v_mfma_f32_16x16x32_bf16 v[18:21], v[210:213], v[162:165], v[18:21]
	v_mfma_f32_16x16x32_bf16 v[6:9], v[198:201], v[170:173], v[6:9]
	v_mfma_f32_16x16x32_bf16 v[2:5], v[210:213], v[170:173], v[2:5]
	v_mfma_f32_16x16x32_bf16 v[54:57], v[206:209], v[150:153], v[54:57]
	v_mfma_f32_16x16x32_bf16 v[50:53], v[232:235], v[150:153], v[50:53]
	v_mfma_f32_16x16x32_bf16 v[38:41], v[206:209], v[158:161], v[38:41]
	v_mfma_f32_16x16x32_bf16 v[34:37], v[232:235], v[158:161], v[34:37]
	v_mfma_f32_16x16x32_bf16 v[22:25], v[206:209], v[166:169], v[22:25]
	v_mfma_f32_16x16x32_bf16 v[18:21], v[232:235], v[166:169], v[18:21]
	v_mfma_f32_16x16x32_bf16 v[6:9], v[206:209], v[174:177], v[6:9]
	v_mfma_f32_16x16x32_bf16 v[2:5], v[232:235], v[174:177], v[2:5]
	s_add_i32 s25, s25, 2
	s_cmp_gt_u32 s25, 5
	s_cbranch_scc1 .Lg2x
	s_barrier
	s_mov_b64 s[26:27], s[28:29]
	s_branch .LBB0_1476
;     __device__ __forceinline__ void operator()(const f32x4 (&acc)[2][2][4][2], const Unit& u, int wr, int wc, int fr, int fq) const {
;     ...
;         float gt[2][4];
; #pragma unroll
;         for (int ai = 0; ai < 2; ++ai)
; #pragma unroll
;             for (int m = 0; m < 4; ++m) gt[ai][m] = gate[u.loff + min(row0 + ai * HALF + m * 16, u.rend - 1)];
; #pragma unroll
;         for (int ai = 0; ai < 2; ++ai)
; #pragma unroll
;             for (int m = 0; m < 4; ++m) { const int row = row0 + ai * HALF + m * 16; if (row < u.rend) { const float g = gt[ai][m]; bf16_t* rowp = Y + (size_t)row * D + col0;
.Lg2x:
	v_add_u32_e32 v160, v227, v178
	v_add_u32_e32 v133, -1, v179
	v_add_u32_e32 v158, 16, v160
	v_min_i32_e32 v130, v158, v133
	v_add_u32_e32 v130, v226, v130
	v_ashrrev_i32_e32 v131, 31, v130
	v_lshl_add_u64 v[130:131], v[130:131], 2, s[20:21]
	v_add_u32_e32 v154, 32, v160
	global_load_dword v156, v[130:131], off
	v_min_i32_e32 v130, v154, v133
	v_add_u32_e32 v130, v226, v130
	v_ashrrev_i32_e32 v131, 31, v130
	v_lshl_add_u64 v[130:131], v[130:131], 2, s[20:21]
	v_add_u32_e32 v150, 48, v160
	global_load_dword v152, v[130:131], off
	v_min_i32_e32 v130, v150, v133
	v_add_u32_e32 v130, v226, v130
	v_ashrrev_i32_e32 v131, 31, v130
	v_lshl_add_u64 v[130:131], v[130:131], 2, s[20:21]
	v_add_u32_e32 v146, 0x80, v160
	global_load_dword v148, v[130:131], off
	v_min_i32_e32 v130, v146, v133
	v_add_u32_e32 v130, v226, v130
	v_ashrrev_i32_e32 v131, 31, v130
	v_lshl_add_u64 v[130:131], v[130:131], 2, s[20:21]
	v_add_u32_e32 v142, 0x90, v160
	global_load_dword v144, v[130:131], off
	v_min_i32_e32 v130, v142, v133
	v_add_u32_e32 v130, v226, v130
	v_ashrrev_i32_e32 v131, 31, v130
	v_lshl_add_u64 v[130:131], v[130:131], 2, s[20:21]
	v_add_u32_e32 v138, 0xa0, v160
	global_load_dword v140, v[130:131], off
	v_min_i32_e32 v130, v138, v133
	v_add_u32_e32 v130, v226, v130
	v_ashrrev_i32_e32 v131, 31, v130
	v_lshl_add_u64 v[130:131], v[130:131], 2, s[20:21]
	v_add_u32_e32 v132, 0xb0, v160
	global_load_dword v134, v[130:131], off
	v_min_i32_e32 v130, v132, v133
	v_add_u32_e32 v130, v226, v130
	v_ashrrev_i32_e32 v131, 31, v130
	v_lshl_add_u64 v[130:131], v[130:131], 2, s[20:21]
	global_load_dword v130, v[130:131], off
	s_barrier
.LBB0_1481:
	v_lshl_or_b32 v136, s16, 8, v224
	v_ashrrev_i32_e32 v137, 31, v136
	v_cmp_lt_i32_e32 vcc, v160, v179
	s_and_saveexec_b64 s[0:1], vcc
	s_cbranch_execnz .LBB0_1489
	s_or_b64 exec, exec, s[0:1]
	v_cmp_lt_i32_e32 vcc, v158, v179
	s_and_saveexec_b64 s[0:1], vcc
	s_cbranch_execnz .LBB0_1490
